# v30 + pool_diff loop rewrite + moe_layout batching + LN head wait + QKV epilogue prefetch (all earlier validated edits stacked)
# speedup vs baseline: 1.0205x; 1.0125x over previous
.LBB0_412:
	s_cmp_lt_i32 s92, 3
	s_cselect_b64 s[2:3], -1, 0
	s_and_b64 s[4:5], s[2:3], s[0:1]
	s_andn2_b64 vcc, exec, s[4:5]
	s_cbranch_vccnz .LBB0_428
	s_lshl_b32 s0, s90, 3
	s_add_i32 s6, s0, s89
	s_add_i32 s0, 0, 0x23aa8
	s_add_i32 s1, 0, 0x23aac
	s_add_i32 s2, 0, 0x23ab0
	s_add_i32 s3, 0, 0x23ab4
	v_mov_b32_e32 v0, s0
	v_mov_b32_e32 v1, s1
	v_mov_b32_e32 v2, s2
	v_mov_b32_e32 v3, s3
	ds_read_b32 v0, v0
	ds_read_b32 v1, v1
	ds_read_b32 v2, v2
	ds_read_b32 v3, v3
	s_cmpk_gt_i32 s6, 0x3fff
	s_waitcnt lgkmcnt(3)
	v_readfirstlane_b32 s0, v0
	s_waitcnt lgkmcnt(2)
	v_readfirstlane_b32 s1, v1
	s_waitcnt lgkmcnt(1)
	v_readfirstlane_b32 s2, v2
	s_waitcnt lgkmcnt(0)
	v_readfirstlane_b32 s3, v3
	v_mbcnt_lo_u32_b32 v22, -1, 0
	v_mbcnt_hi_u32_b32 v22, -1, v22
	s_cbranch_scc1 .LBB0_418
	s_ashr_i32 s7, s6, 31
	s_lshl_b32 s8, s87, 3
	s_lshl_b64 s[12:13], s[6:7], 12
	s_waitcnt vmcnt(11)
	v_lshlrev_b32_e32 v24, 2, v22
	s_add_u32 s10, s64, s12
	v_ashrrev_i32_e32 v25, 31, v24
	s_addc_u32 s11, s65, s13
	v_lshlrev_b64 v[42:43], 1, v[24:25]
	v_lshl_add_u64 v[0:1], s[10:11], 0, v[42:43]
	global_load_dwordx2 v[34:35], v[0:1], off
	global_load_dwordx2 v[36:37], v[0:1], off offset:512
	global_load_dwordx2 v[38:39], v[0:1], off offset:1024
	global_load_dwordx2 v[26:27], v[0:1], off offset:1536
	global_load_dwordx2 v[32:33], v[0:1], off offset:2048
	global_load_dwordx2 v[40:41], v[0:1], off offset:2560
	global_load_dwordx2 v[28:29], v[0:1], off offset:3072
	global_load_dwordx2 v[30:31], v[0:1], off offset:3584
	v_mbcnt_lo_u32_b32 v2, -1, 0
	v_mbcnt_hi_u32_b32 v2, -1, v2
	v_and_b32_e32 v3, 64, v2
	v_add_u32_e32 v3, 64, v3
	v_xor_b32_e32 v4, 1, v2
	v_cmp_lt_i32_e32 vcc, v4, v3
	v_lshl_add_u64 v[0:1], s[64:65], 0, v[42:43]
	v_mov_b32_e32 v72, 0x3727c5ac
	v_cndmask_b32_e32 v4, v2, v4, vcc
	v_lshlrev_b32_e32 v66, 2, v4
	v_xor_b32_e32 v4, 2, v2
	v_cmp_lt_i32_e32 vcc, v4, v3
	v_mov_b32_e32 v73, 0x260
	s_mov_b32 s20, 0x30a00000
	v_cndmask_b32_e32 v4, v2, v4, vcc
	v_lshlrev_b32_e32 v67, 2, v4
	v_xor_b32_e32 v4, 4, v2
	v_cmp_lt_i32_e32 vcc, v4, v3
	s_mov_b32 s21, 0xc0c0400
	s_mov_b32 s22, 0x4000c0c
	v_cndmask_b32_e32 v4, v2, v4, vcc
	s_waitcnt vmcnt(17)
	v_lshlrev_b32_e32 v68, 2, v4
	v_xor_b32_e32 v4, 8, v2
	v_cmp_lt_i32_e32 vcc, v4, v3
	s_mov_b32 s23, 0x38a00000
	v_mov_b32_e32 v74, 0
	v_cndmask_b32_e32 v4, v2, v4, vcc
	v_lshlrev_b32_e32 v69, 2, v4
	v_xor_b32_e32 v4, 16, v2
	v_cmp_lt_i32_e32 vcc, v4, v3
	s_nop 1
	v_cndmask_b32_e32 v4, v2, v4, vcc
	v_lshlrev_b32_e32 v70, 2, v4
	v_xor_b32_e32 v4, 32, v2
	v_cmp_lt_i32_e32 vcc, v4, v3
	s_nop 1
	v_cndmask_b32_e32 v2, v2, v4, vcc
	v_lshlrev_b64 v[4:5], 2, v[24:25]
	v_lshlrev_b32_e32 v71, 2, v2
	v_lshl_add_u64 v[2:3], s[0:1], 0, v[4:5]
	v_lshl_add_u64 v[4:5], s[2:3], 0, v[4:5]
	s_mov_b64 s[0:1], 0x1000
	v_lshl_add_u64 v[6:7], v[2:3], 0, s[0:1]
	v_lshl_add_u64 v[8:9], v[4:5], 0, s[0:1]
	s_mov_b64 s[0:1], 0x1400
	s_lshl_b64 s[2:3], s[6:7], 2
	v_lshl_add_u64 v[10:11], v[2:3], 0, s[0:1]
	v_lshl_add_u64 v[12:13], v[4:5], 0, s[0:1]
	s_mov_b64 s[0:1], 0x1800
	s_add_u32 s18, s2, 0x518000
	v_lshl_add_u64 v[14:15], v[2:3], 0, s[0:1]
	v_lshl_add_u64 v[16:17], v[4:5], 0, s[0:1]
	s_mov_b64 s[0:1], 0x1c00
	s_addc_u32 s19, s3, 0
	s_ashr_i32 s9, s8, 31
	s_lshl_b64 s[2:3], s[6:7], 11
	v_lshl_add_u64 v[18:19], v[2:3], 0, s[0:1]
	v_lshl_add_u64 v[20:21], v[4:5], 0, s[0:1]
	v_cmp_eq_u32_e64 s[0:1], 0, v22
	s_lshl_b64 s[10:11], s[8:9], 2
	v_lshl_add_u64 v[22:23], s[12:13], 0, v[42:43]
	s_lshl_b64 s[12:13], s[8:9], 12
	v_lshl_add_u64 v[24:25], s[2:3], 0, v[24:25]
	s_lshl_b64 s[14:15], s[8:9], 11
	s_mov_b32 s7, 0xf800000
	s_mov_b32 s9, 0x42fe0000
	s_waitcnt vmcnt(0)
	s_branch .LBB0_416

.LBB0_416:
	s_waitcnt vmcnt(23)
	v_mov_b64_e32 v[50:51], v[34:35]
	s_waitcnt vmcnt(22)
	v_mov_b64_e32 v[56:57], v[36:37]
	v_lshlrev_b32_e32 v59, 16, v50
	v_lshlrev_b32_e32 v58, 16, v56
	v_and_b32_e32 v61, 0xffff0000, v50
	v_and_b32_e32 v60, 0xffff0000, v56
	v_lshlrev_b32_e32 v53, 16, v51
	v_lshlrev_b32_e32 v52, 16, v57
	v_and_b32_e32 v55, 0xffff0000, v51
	v_and_b32_e32 v54, 0xffff0000, v57
	v_pk_add_f32 v[50:51], v[58:59], v[60:61]
	v_pk_add_f32 v[56:57], v[52:53], v[54:55]
	s_waitcnt vmcnt(21)
	v_mov_b64_e32 v[62:63], v[38:39]
	v_pk_add_f32 v[50:51], v[50:51], v[56:57]
	s_waitcnt vmcnt(20)
	v_lshlrev_b32_e32 v44, 16, v27
	v_and_b32_e32 v45, 0xffff0000, v27
	v_add_f32_e32 v27, 0, v51
	v_add_f32_e32 v47, v50, v27
	v_lshlrev_b32_e32 v51, 16, v63
	v_lshlrev_b32_e32 v50, 16, v62
	v_and_b32_e32 v77, 0xffff0000, v63
	v_and_b32_e32 v76, 0xffff0000, v62
	v_pk_add_f32 v[56:57], v[50:51], v[76:77]
	v_lshlrev_b32_e32 v42, 16, v26
	v_and_b32_e32 v43, 0xffff0000, v26
	v_pk_add_f32 v[56:57], v[56:57], v[56:57] op_sel_hi:[0,1]
	s_waitcnt vmcnt(18)
	v_mov_b64_e32 v[64:65], v[40:41]
	v_lshlrev_b32_e32 v40, 16, v32
	v_and_b32_e32 v48, 0xffff0000, v32
	v_lshlrev_b32_e32 v38, 16, v33
	v_and_b32_e32 v46, 0xffff0000, v33
	v_add_f32_e32 v41, v42, v43
	v_add_f32_e32 v49, v44, v45
	v_mov_b32_e32 v39, v57
	v_pk_add_f32 v[62:63], v[40:41], v[48:49]
	v_pk_add_f32 v[56:57], v[38:39], v[46:47]
	v_and_b32_e32 v79, 0xffff0000, v65
	v_pk_add_f32 v[56:57], v[62:63], v[56:57]
	v_and_b32_e32 v78, 0xffff0000, v64
	v_pk_add_f32 v[62:63], v[56:57], v[56:57] op_sel_hi:[0,1]
	v_lshlrev_b32_e32 v57, 16, v65
	v_lshlrev_b32_e32 v56, 16, v64
	v_pk_add_f32 v[64:65], v[56:57], v[78:79]
	s_waitcnt vmcnt(17)
	v_lshlrev_b32_e32 v32, 16, v28
	v_and_b32_e32 v33, 0xffff0000, v28
	v_lshlrev_b32_e32 v36, 16, v29
	v_and_b32_e32 v37, 0xffff0000, v29
	v_pk_add_f32 v[64:65], v[64:65], v[64:65] op_sel_hi:[0,1]
	s_waitcnt vmcnt(16)
	v_lshlrev_b32_e32 v28, 16, v30
	v_and_b32_e32 v34, 0xffff0000, v30
	v_lshlrev_b32_e32 v26, 16, v31
	v_and_b32_e32 v30, 0xffff0000, v31
	v_add_f32_e32 v29, v32, v33
	v_add_f32_e32 v35, v36, v37
	v_mov_b32_e32 v27, v65
	v_mov_b32_e32 v31, v63
	v_pk_add_f32 v[80:81], v[28:29], v[34:35]
	v_pk_add_f32 v[62:63], v[26:27], v[30:31]
	s_nop 0
	v_pk_add_f32 v[62:63], v[80:81], v[62:63]
	s_nop 0
	v_add_f32_e32 v27, v62, v63
	ds_bpermute_b32 v29, v66, v27
	s_waitcnt lgkmcnt(0)
	v_add_f32_e32 v27, v27, v29
	ds_bpermute_b32 v29, v67, v27
	s_waitcnt lgkmcnt(0)
	v_add_f32_e32 v27, v27, v29
	ds_bpermute_b32 v29, v68, v27
	s_waitcnt lgkmcnt(0)
	v_add_f32_e32 v27, v27, v29
	ds_bpermute_b32 v29, v69, v27
	s_waitcnt lgkmcnt(0)
	v_add_f32_e32 v27, v27, v29
	ds_bpermute_b32 v29, v70, v27
	s_waitcnt lgkmcnt(0)
	v_add_f32_e32 v27, v27, v29
	ds_bpermute_b32 v29, v71, v27
	s_waitcnt lgkmcnt(0)
	v_add_f32_e32 v27, v27, v29
	v_fmac_f32_e32 v61, 0xba000000, v27
	v_fmac_f32_e32 v60, 0xba000000, v27
	v_fmac_f32_e32 v55, 0xba000000, v27
	v_fmac_f32_e32 v59, 0xba000000, v27
	v_fmac_f32_e32 v54, 0xba000000, v27
	v_fmac_f32_e32 v58, 0xba000000, v27
	v_mov_b32_e32 v64, v61
	v_mov_b32_e32 v65, v60
	v_fmac_f32_e32 v53, 0xba000000, v27
	v_fmac_f32_e32 v52, 0xba000000, v27
	v_mov_b32_e32 v62, v59
	v_mov_b32_e32 v63, v58
	v_pk_mul_f32 v[64:65], v[64:65], v[64:65]
	v_mov_b32_e32 v80, v55
	v_mov_b32_e32 v81, v54
	v_pk_fma_f32 v[62:63], v[62:63], v[62:63], v[64:65]
	v_mov_b32_e32 v64, v53
	v_mov_b32_e32 v65, v52
	v_pk_mul_f32 v[80:81], v[80:81], v[80:81]
	v_fmac_f32_e32 v76, 0xba000000, v27
	v_pk_fma_f32 v[64:65], v[64:65], v[64:65], v[80:81]
	v_fmac_f32_e32 v77, 0xba000000, v27
	v_pk_add_f32 v[62:63], v[62:63], v[64:65]
	v_fmac_f32_e32 v51, 0xba000000, v27
	v_pk_add_f32 v[64:65], v[62:63], v[62:63] op_sel_hi:[0,1]
	v_fmac_f32_e32 v50, 0xba000000, v27
	v_mov_b32_e32 v62, v51
	v_mov_b32_e32 v63, v77
	v_mov_b32_e32 v51, v76
	v_pk_mul_f32 v[80:81], v[62:63], v[62:63]
	v_pk_mul_f32 v[76:77], v[50:51], v[50:51]
	v_fmac_f32_e32 v42, 0xba000000, v27
	v_pk_mov_b32 v[82:83], v[76:77], v[80:81] op_sel:[1,0]
	v_mov_b32_e32 v77, v81
	v_fmac_f32_e32 v43, 0xba000000, v27
	v_fmac_f32_e32 v44, 0xba000000, v27
	v_mul_f32_e32 v64, v42, v42
	v_pk_add_f32 v[76:77], v[82:83], v[76:77]
	v_fmac_f32_e32 v45, 0xba000000, v27
	v_pk_fma_f32 v[80:81], v[42:43], v[42:43], v[64:65] op_sel_hi:[1,1,0]
	v_mul_f32_e32 v64, v44, v44
	v_pk_add_f32 v[76:77], v[76:77], v[76:77] op_sel_hi:[0,1]
	v_pk_fma_f32 v[82:83], v[44:45], v[44:45], v[64:65] op_sel_hi:[1,1,0]
	v_fmac_f32_e32 v46, 0xba000000, v27
	v_fmac_f32_e32 v38, 0xba000000, v27
	v_fmac_f32_e32 v48, 0xba000000, v27
	v_fmac_f32_e32 v40, 0xba000000, v27
	v_mul_f32_e32 v80, v40, v40
	v_mul_f32_e32 v82, v48, v48
	v_mul_f32_e32 v76, v38, v38
	v_mul_f32_e32 v64, v46, v46
	v_pk_add_f32 v[80:81], v[80:81], v[82:83]
	v_pk_add_f32 v[64:65], v[76:77], v[64:65]
	v_fmac_f32_e32 v78, 0xba000000, v27
	v_pk_add_f32 v[64:65], v[80:81], v[64:65]
	v_fmac_f32_e32 v79, 0xba000000, v27
	v_fmac_f32_e32 v57, 0xba000000, v27
	v_pk_add_f32 v[76:77], v[64:65], v[64:65] op_sel_hi:[0,1]
	v_fmac_f32_e32 v56, 0xba000000, v27
	v_mov_b32_e32 v64, v57
	v_mov_b32_e32 v65, v79
	v_mov_b32_e32 v57, v78
	v_pk_mul_f32 v[80:81], v[64:65], v[64:65]
	v_pk_mul_f32 v[78:79], v[56:57], v[56:57]
	v_fmac_f32_e32 v32, 0xba000000, v27
	v_pk_mov_b32 v[82:83], v[78:79], v[80:81] op_sel:[1,0]
	v_mov_b32_e32 v79, v81
	v_fmac_f32_e32 v33, 0xba000000, v27
	v_fmac_f32_e32 v36, 0xba000000, v27
	v_mul_f32_e32 v76, v32, v32
	v_pk_add_f32 v[78:79], v[82:83], v[78:79]
	v_fmac_f32_e32 v37, 0xba000000, v27
	v_pk_fma_f32 v[80:81], v[32:33], v[32:33], v[76:77] op_sel_hi:[1,1,0]
	v_mul_f32_e32 v76, v36, v36
	v_pk_add_f32 v[78:79], v[78:79], v[78:79] op_sel_hi:[0,1]
	v_pk_fma_f32 v[82:83], v[36:37], v[36:37], v[76:77] op_sel_hi:[1,1,0]
	v_fmac_f32_e32 v30, 0xba000000, v27
	v_fmac_f32_e32 v26, 0xba000000, v27
	v_fmac_f32_e32 v34, 0xba000000, v27
	v_fmac_f32_e32 v28, 0xba000000, v27
	v_mul_f32_e32 v80, v28, v28
	v_mul_f32_e32 v82, v34, v34
	v_mul_f32_e32 v78, v26, v26
	v_mul_f32_e32 v76, v30, v30
	v_pk_add_f32 v[80:81], v[80:81], v[82:83]
	v_pk_add_f32 v[76:77], v[78:79], v[76:77]
	v_mov_b32_e32 v140, v58
	v_pk_add_f32 v[76:77], v[80:81], v[76:77]
	v_mov_b32_e32 v141, v60
	v_add_f32_e32 v27, v76, v77
	global_load_dwordx4 v[76:79], v[2:3], off
	global_load_dwordx4 v[80:83], v[4:5], off
	global_load_dwordx4 v[84:87], v[2:3], off offset:1024
	global_load_dwordx4 v[88:91], v[4:5], off offset:1024
	global_load_dwordx4 v[92:95], v[2:3], off offset:2048
	global_load_dwordx4 v[96:99], v[4:5], off offset:2048
	global_load_dwordx4 v[100:103], v[2:3], off offset:3072
	global_load_dwordx4 v[104:107], v[4:5], off offset:3072
	global_load_dwordx4 v[108:111], v[6:7], off
	global_load_dwordx4 v[112:115], v[8:9], off
	global_load_dwordx4 v[116:119], v[10:11], off
	global_load_dwordx4 v[120:123], v[12:13], off
	global_load_dwordx4 v[124:127], v[14:15], off
	global_load_dwordx4 v[128:131], v[16:17], off
	global_load_dwordx4 v[132:135], v[18:19], off
	global_load_dwordx4 v[136:139], v[20:21], off
	ds_bpermute_b32 v29, v66, v27
	v_mov_b32_e32 v60, v59
	v_mov_b32_e32 v58, v52
	v_mov_b32_e32 v59, v54
	v_mov_b32_e32 v54, v53
	s_waitcnt lgkmcnt(0)
	v_add_f32_e32 v27, v27, v29
	ds_bpermute_b32 v29, v67, v27
	s_waitcnt lgkmcnt(0)
	v_add_f32_e32 v27, v27, v29
	ds_bpermute_b32 v29, v68, v27
	s_waitcnt lgkmcnt(0)
	v_add_f32_e32 v27, v27, v29
	ds_bpermute_b32 v29, v69, v27
	s_waitcnt lgkmcnt(0)
	v_add_f32_e32 v27, v27, v29
	ds_bpermute_b32 v29, v70, v27
	s_waitcnt lgkmcnt(0)
	v_add_f32_e32 v27, v27, v29
	ds_bpermute_b32 v29, v71, v27
	s_waitcnt lgkmcnt(0)
	v_add_f32_e32 v27, v27, v29
	v_fmamk_f32 v27, v27, 0x3a000000, v72
	v_mul_f32_e32 v29, 0x4f800000, v27
	v_cmp_gt_f32_e32 vcc, s7, v27
	s_nop 1
	v_cndmask_b32_e32 v27, v27, v29, vcc
	v_sqrt_f32_e32 v29, v27
	s_nop 0
	v_add_u32_e32 v31, -1, v29
	v_fma_f32 v35, -v31, v29, v27
	v_cmp_ge_f32_e64 s[2:3], 0, v35
	v_add_u32_e32 v35, 1, v29
	s_nop 0
	v_cndmask_b32_e64 v31, v29, v31, s[2:3]
	v_fma_f32 v29, -v35, v29, v27
	v_cmp_lt_f32_e64 s[2:3], 0, v29
	s_nop 1
	v_cndmask_b32_e64 v29, v31, v35, s[2:3]
	v_mul_f32_e32 v31, 0x37800000, v29
	v_cndmask_b32_e32 v29, v29, v31, vcc
	v_cmp_class_f32_e32 vcc, v27, v73
	s_nop 1
	v_cndmask_b32_e32 v27, v29, v27, vcc
	v_div_scale_f32 v29, s[2:3], v27, v27, 1.0
	v_rcp_f32_e32 v31, v29
	s_mov_b32 s2, s6
	s_add_i32 s6, s6, s8
	s_cmpk_gt_i32 s6, 0x3fff
	v_fma_f32 v35, -v29, v31, 1.0
	v_fmac_f32_e32 v31, v35, v31
	v_div_scale_f32 v35, vcc, 1.0, v27, 1.0
	v_mul_f32_e32 v39, v35, v31
	v_fma_f32 v41, -v29, v39, v35
	v_fmac_f32_e32 v39, v41, v31
	v_fma_f32 v29, -v29, v39, v35
	v_div_fmas_f32 v29, v29, v31, v39
	v_div_fixup_f32 v52, v29, v27, 1.0
	v_pk_mul_f32 v[60:61], v[60:61], v[52:53] op_sel_hi:[1,0]
	v_pk_mul_f32 v[54:55], v[54:55], v[52:53] op_sel_hi:[1,0]
	v_mov_b32_e32 v41, v48
	v_mov_b32_e32 v39, v46
	v_mov_b32_e32 v27, v30
	s_waitcnt vmcnt(14)
	v_pk_fma_f32 v[54:55], v[78:79], v[54:55], v[82:83]
	v_pk_fma_f32 v[60:61], v[76:77], v[60:61], v[80:81]
	v_pk_mul_f32 v[76:77], v[140:141], v[52:53] op_sel_hi:[1,0]
	v_pk_mul_f32 v[58:59], v[58:59], v[52:53] op_sel_hi:[1,0]
	v_pk_mul_f32 v[40:41], v[40:41], v[52:53] op_sel_hi:[1,0]
	v_pk_mul_f32 v[38:39], v[38:39], v[52:53] op_sel_hi:[1,0]
	v_mov_b32_e32 v29, v34
	v_pk_mul_f32 v[26:27], v[26:27], v[52:53] op_sel_hi:[1,0]
	s_waitcnt vmcnt(12)
	v_pk_fma_f32 v[58:59], v[86:87], v[58:59], v[90:91]
	v_pk_fma_f32 v[76:77], v[84:85], v[76:77], v[88:89]
	v_pk_mul_f32 v[50:51], v[50:51], v[52:53] op_sel_hi:[1,0]
	v_pk_mul_f32 v[62:63], v[62:63], v[52:53] op_sel_hi:[1,0]
	v_pk_mul_f32 v[42:43], v[42:43], v[52:53] op_sel_hi:[1,0]
	v_pk_mul_f32 v[44:45], v[44:45], v[52:53] op_sel_hi:[1,0]
	s_waitcnt vmcnt(6)
	v_pk_fma_f32 v[46:47], v[110:111], v[38:39], v[114:115]
	v_pk_fma_f32 v[48:49], v[108:109], v[40:41], v[112:113]
	v_pk_mul_f32 v[38:39], v[56:57], v[52:53] op_sel_hi:[1,0]
	v_pk_mul_f32 v[40:41], v[64:65], v[52:53] op_sel_hi:[1,0]
	v_pk_mul_f32 v[32:33], v[32:33], v[52:53] op_sel_hi:[1,0]
	v_pk_mul_f32 v[36:37], v[36:37], v[52:53] op_sel_hi:[1,0]
	v_pk_mul_f32 v[28:29], v[28:29], v[52:53] op_sel_hi:[1,0]
	s_waitcnt vmcnt(0)
	v_pk_fma_f32 v[52:53], v[134:135], v[26:27], v[138:139]
	v_max_f32_e64 v26, |v60|, |v61|
	v_max_f32_e64 v27, |v54|, |v55|
	v_pk_fma_f32 v[62:63], v[94:95], v[62:63], v[98:99]
	v_pk_fma_f32 v[50:51], v[92:93], v[50:51], v[96:97]
	v_pk_fma_f32 v[84:85], v[132:133], v[28:29], v[136:137]
	v_max3_f32 v26, v26, 0, v27
	v_max_f32_e64 v27, |v76|, |v77|
	v_max_f32_e64 v28, |v58|, |v59|
	v_pk_fma_f32 v[44:45], v[102:103], v[44:45], v[106:107]
	v_pk_fma_f32 v[78:79], v[100:101], v[42:43], v[104:105]
	v_max3_f32 v26, v26, v27, v28
	v_max_f32_e64 v27, |v50|, |v51|
	v_max_f32_e64 v28, |v62|, |v63|
	v_max3_f32 v26, v26, v27, v28
	v_max_f32_e64 v27, |v78|, |v79|
	v_max_f32_e64 v28, |v44|, |v45|
	v_pk_fma_f32 v[56:57], v[118:119], v[40:41], v[122:123]
	v_pk_fma_f32 v[64:65], v[116:117], v[38:39], v[120:121]
	v_max3_f32 v26, v26, v27, v28
	v_max_f32_e64 v27, |v48|, |v49|
	v_max_f32_e64 v28, |v46|, |v47|
	v_pk_fma_f32 v[80:81], v[126:127], v[36:37], v[130:131]
	v_pk_fma_f32 v[82:83], v[124:125], v[32:33], v[128:129]
	v_max3_f32 v26, v26, v27, v28
	v_max_f32_e64 v27, |v64|, |v65|
	v_max_f32_e64 v28, |v56|, |v57|
	v_max3_f32 v26, v26, v27, v28
	v_max_f32_e64 v27, |v82|, |v83|
	v_max_f32_e64 v28, |v80|, |v81|
	v_max3_f32 v26, v26, v27, v28
	v_max_f32_e64 v27, |v84|, |v85|
	v_max_f32_e64 v28, |v52|, |v53|
	v_max3_f32 v26, v26, v27, v28
	ds_bpermute_b32 v27, v66, v26
	s_cselect_b64 s[16:17], -1, 0
	s_cmpk_lt_i32 s6, 0x4000
	s_cselect_b32 s2, s6, s2
	s_ashr_i32 s3, s2, 31
	s_waitcnt lgkmcnt(0)
	v_max_f32_e32 v27, v27, v27
	v_max_f32_e32 v26, v26, v27
	ds_bpermute_b32 v27, v67, v26
	s_lshl_b64 s[2:3], s[2:3], 12
	v_lshl_add_u64 v[86:87], v[0:1], 0, s[2:3]
	s_waitcnt lgkmcnt(0)
	v_max_f32_e32 v27, v27, v27
	v_max_f32_e32 v26, v26, v27
	ds_bpermute_b32 v27, v68, v26
	s_waitcnt lgkmcnt(0)
	v_max_f32_e32 v27, v27, v27
	v_max_f32_e32 v26, v26, v27
	ds_bpermute_b32 v27, v69, v26
	s_waitcnt lgkmcnt(0)
	v_max_f32_e32 v27, v27, v27
	v_max_f32_e32 v26, v26, v27
	ds_bpermute_b32 v27, v70, v26
	s_waitcnt lgkmcnt(0)
	v_max_f32_e32 v27, v27, v27
	v_max_f32_e32 v28, v26, v27
	ds_bpermute_b32 v29, v71, v28
	global_load_dwordx2 v[34:35], v[86:87], off
	global_load_dwordx2 v[36:37], v[86:87], off offset:512
	global_load_dwordx2 v[38:39], v[86:87], off offset:1024
	global_load_dwordx2 v[26:27], v[86:87], off offset:1536
	s_waitcnt lgkmcnt(0)
	v_max_f32_e32 v29, v29, v29
	v_max_f32_e32 v42, v28, v29
	global_load_dwordx2 v[32:33], v[86:87], off offset:2048
	global_load_dwordx2 v[40:41], v[86:87], off offset:2560
	global_load_dwordx2 v[28:29], v[86:87], off offset:3072
	global_load_dwordx2 v[30:31], v[86:87], off offset:3584
	v_div_scale_f32 v43, s[2:3], v42, v42, s9
	v_rcp_f32_e32 v75, v43
	v_cvt_pk_bf16_f32 v90, v60, v61
	v_cvt_pk_bf16_f32 v91, v54, v55
	s_nop 0
	v_fma_f32 v86, -v43, v75, 1.0
	v_fmac_f32_e32 v75, v86, v75
	v_div_scale_f32 v86, vcc, s9, v42, s9
	v_mul_f32_e32 v87, v86, v75
	v_fma_f32 v88, -v43, v87, v86
	v_fmac_f32_e32 v87, v88, v75
	v_fma_f32 v43, -v43, v87, v86
	v_div_fmas_f32 v43, v43, v75, v87
	v_div_fixup_f32 v43, v43, v42, s9
	v_cmp_lt_f32_e32 vcc, 0, v42
	v_lshl_add_u64 v[86:87], s[66:67], 0, v[22:23]
	v_add_co_u32_e64 v86, s[2:3], s20, v86
	v_cndmask_b32_e32 v43, 0, v43, vcc
	v_fmaak_f32 v60, v60, v43, 0x4b400000
	v_fmaak_f32 v61, v61, v43, 0x4b400000
	v_fmaak_f32 v54, v54, v43, 0x4b400000
	v_fmaak_f32 v55, v55, v43, 0x4b400000
	v_lshl_add_u64 v[88:89], s[66:67], 0, v[24:25]
	v_addc_co_u32_e64 v87, s[2:3], 0, v87, s[2:3]
	v_perm_b32 v60, v61, v60, s21
	v_perm_b32 v54, v55, v54, s22
	v_or_b32_e32 v60, v54, v60
	v_add_co_u32_e64 v54, s[2:3], s23, v88
	global_store_dwordx2 v[86:87], v[90:91], off
	s_nop 0
	v_addc_co_u32_e64 v55, s[2:3], 0, v89, s[2:3]
	global_store_dword v[54:55], v60, off
	v_cvt_pk_bf16_f32 v60, v76, v77
	v_cvt_pk_bf16_f32 v61, v58, v59
	global_store_dwordx2 v[86:87], v[60:61], off offset:512
	v_fmaak_f32 v60, v76, v43, 0x4b400000
	v_fmaak_f32 v61, v77, v43, 0x4b400000
	v_fmaak_f32 v58, v58, v43, 0x4b400000
	v_fmaak_f32 v59, v59, v43, 0x4b400000
	v_perm_b32 v60, v61, v60, s21
	v_perm_b32 v58, v59, v58, s22
	v_or_b32_e32 v58, v58, v60
	global_store_dword v[54:55], v58, off offset:256
	v_cvt_pk_bf16_f32 v58, v50, v51
	v_cvt_pk_bf16_f32 v59, v62, v63
	global_store_dwordx2 v[86:87], v[58:59], off offset:1024
	v_fmaak_f32 v50, v50, v43, 0x4b400000
	v_fmaak_f32 v51, v51, v43, 0x4b400000
	v_fmaak_f32 v58, v62, v43, 0x4b400000
	v_fmaak_f32 v59, v63, v43, 0x4b400000
	v_perm_b32 v50, v51, v50, s21
	v_perm_b32 v51, v59, v58, s22
	v_or_b32_e32 v50, v51, v50
	global_store_dword v[54:55], v50, off offset:512
	v_cvt_pk_bf16_f32 v50, v78, v79
	v_cvt_pk_bf16_f32 v51, v44, v45
	global_store_dwordx2 v[86:87], v[50:51], off offset:1536
	v_fmaak_f32 v50, v78, v43, 0x4b400000
	v_fmaak_f32 v51, v79, v43, 0x4b400000
	v_fmaak_f32 v44, v44, v43, 0x4b400000
	v_fmaak_f32 v45, v45, v43, 0x4b400000
	v_perm_b32 v50, v51, v50, s21
	v_perm_b32 v44, v45, v44, s22
	v_or_b32_e32 v44, v44, v50
	global_store_dword v[54:55], v44, off offset:768
	v_cvt_pk_bf16_f32 v44, v48, v49
	v_cvt_pk_bf16_f32 v45, v46, v47
	global_store_dwordx2 v[86:87], v[44:45], off offset:2048
	v_fmaak_f32 v44, v48, v43, 0x4b400000
	v_fmaak_f32 v45, v49, v43, 0x4b400000
	v_fmaak_f32 v46, v46, v43, 0x4b400000
	v_fmaak_f32 v47, v47, v43, 0x4b400000
	v_perm_b32 v44, v45, v44, s21
	v_perm_b32 v45, v47, v46, s22
	v_or_b32_e32 v44, v45, v44
	global_store_dword v[54:55], v44, off offset:1024
	v_cvt_pk_bf16_f32 v44, v64, v65
	v_cvt_pk_bf16_f32 v45, v56, v57
	global_store_dwordx2 v[86:87], v[44:45], off offset:2560
	v_fmaak_f32 v44, v64, v43, 0x4b400000
	v_fmaak_f32 v45, v65, v43, 0x4b400000
	v_fmaak_f32 v46, v56, v43, 0x4b400000
	v_fmaak_f32 v47, v57, v43, 0x4b400000
	v_perm_b32 v44, v45, v44, s21
	v_perm_b32 v45, v47, v46, s22
	v_or_b32_e32 v44, v45, v44
	global_store_dword v[54:55], v44, off offset:1280
	v_cvt_pk_bf16_f32 v44, v82, v83
	v_cvt_pk_bf16_f32 v45, v80, v81
	global_store_dwordx2 v[86:87], v[44:45], off offset:3072
	v_fmaak_f32 v44, v82, v43, 0x4b400000
	v_fmaak_f32 v45, v83, v43, 0x4b400000
	v_fmaak_f32 v46, v80, v43, 0x4b400000
	v_fmaak_f32 v47, v81, v43, 0x4b400000
	v_perm_b32 v44, v45, v44, s21
	v_perm_b32 v45, v47, v46, s22
	v_or_b32_e32 v44, v45, v44
	global_store_dword v[54:55], v44, off offset:1536
	v_cvt_pk_bf16_f32 v44, v84, v85
	v_cvt_pk_bf16_f32 v45, v52, v53
	global_store_dwordx2 v[86:87], v[44:45], off offset:3584
	v_fmaak_f32 v44, v84, v43, 0x4b400000
	v_fmaak_f32 v45, v85, v43, 0x4b400000
	v_fmaak_f32 v46, v52, v43, 0x4b400000
	v_fmaak_f32 v43, v53, v43, 0x4b400000
	v_perm_b32 v44, v45, v44, s21
	v_perm_b32 v43, v43, v46, s22
	v_or_b32_e32 v43, v43, v44
	global_store_dword v[54:55], v43, off offset:1792
	s_and_saveexec_b64 s[2:3], s[0:1]
	s_cbranch_execz .LBB0_415
	s_add_u32 s24, s66, s18
	v_mul_f32_e32 v42, 0x3c010204, v42
	s_addc_u32 s25, s67, s19
	v_cndmask_b32_e32 v42, 1.0, v42, vcc
	global_store_dword v74, v42, s[24:25]
	s_branch .LBB0_415

.LBB0_634:
	s_cmp_lt_i32 s92, 6
	s_cselect_b64 s[2:3], -1, 0
	s_and_b64 s[4:5], s[2:3], s[0:1]
	s_andn2_b64 vcc, exec, s[4:5]
	s_cbranch_vccnz .LBB0_640
	s_lshl_b32 s0, s90, 3
	s_add_i32 s6, s0, s89
	s_add_i32 s0, 0, 0x23ab8
	s_add_i32 s1, 0, 0x23abc
	s_add_i32 s2, 0, 0x23ac0
	s_add_i32 s3, 0, 0x23ac4
	v_mov_b32_e32 v0, s0
	v_mov_b32_e32 v1, s1
	v_mov_b32_e32 v2, s2
	v_mov_b32_e32 v3, s3
	ds_read_b32 v0, v0
	ds_read_b32 v1, v1
	ds_read_b32 v2, v2
	ds_read_b32 v3, v3
	s_cmpk_gt_i32 s6, 0x3fff
	s_waitcnt lgkmcnt(3)
	v_readfirstlane_b32 s0, v0
	s_waitcnt lgkmcnt(2)
	v_readfirstlane_b32 s1, v1
	s_waitcnt lgkmcnt(1)
	v_readfirstlane_b32 s2, v2
	s_waitcnt lgkmcnt(0)
	v_readfirstlane_b32 s3, v3
	v_mbcnt_lo_u32_b32 v22, -1, 0
	v_mbcnt_hi_u32_b32 v22, -1, v22
	s_cbranch_scc1 .LBB0_640
	s_ashr_i32 s7, s6, 31
	s_lshl_b32 s8, s87, 3
	s_lshl_b64 s[12:13], s[6:7], 12
	s_waitcnt vmcnt(11)
	v_lshlrev_b32_e32 v24, 2, v22
	s_add_u32 s10, s64, s12
	v_ashrrev_i32_e32 v25, 31, v24
	s_addc_u32 s11, s65, s13
	v_lshlrev_b64 v[42:43], 1, v[24:25]
	v_lshl_add_u64 v[0:1], s[10:11], 0, v[42:43]
	global_load_dwordx2 v[34:35], v[0:1], off
	global_load_dwordx2 v[36:37], v[0:1], off offset:512
	global_load_dwordx2 v[38:39], v[0:1], off offset:1024
	global_load_dwordx2 v[26:27], v[0:1], off offset:1536
	global_load_dwordx2 v[32:33], v[0:1], off offset:2048
	global_load_dwordx2 v[40:41], v[0:1], off offset:2560
	global_load_dwordx2 v[28:29], v[0:1], off offset:3072
	global_load_dwordx2 v[30:31], v[0:1], off offset:3584
	v_mbcnt_lo_u32_b32 v2, -1, 0
	v_mbcnt_hi_u32_b32 v2, -1, v2
	v_and_b32_e32 v3, 64, v2
	v_add_u32_e32 v3, 64, v3
	v_xor_b32_e32 v4, 1, v2
	v_cmp_lt_i32_e32 vcc, v4, v3
	v_lshl_add_u64 v[0:1], s[64:65], 0, v[42:43]
	v_mov_b32_e32 v72, 0x3727c5ac
	v_cndmask_b32_e32 v4, v2, v4, vcc
	v_lshlrev_b32_e32 v66, 2, v4
	v_xor_b32_e32 v4, 2, v2
	v_cmp_lt_i32_e32 vcc, v4, v3
	v_mov_b32_e32 v73, 0x260
	s_mov_b32 s20, 0x30a00000
	v_cndmask_b32_e32 v4, v2, v4, vcc
	v_lshlrev_b32_e32 v67, 2, v4
	v_xor_b32_e32 v4, 4, v2
	v_cmp_lt_i32_e32 vcc, v4, v3
	s_mov_b32 s21, 0xc0c0400
	s_mov_b32 s22, 0x4000c0c
	v_cndmask_b32_e32 v4, v2, v4, vcc
	s_waitcnt vmcnt(17)
	v_lshlrev_b32_e32 v68, 2, v4
	v_xor_b32_e32 v4, 8, v2
	v_cmp_lt_i32_e32 vcc, v4, v3
	s_mov_b32 s23, 0x38a00000
	v_mov_b32_e32 v74, 0
	v_cndmask_b32_e32 v4, v2, v4, vcc
	v_lshlrev_b32_e32 v69, 2, v4
	v_xor_b32_e32 v4, 16, v2
	v_cmp_lt_i32_e32 vcc, v4, v3
	s_nop 1
	v_cndmask_b32_e32 v4, v2, v4, vcc
	v_lshlrev_b32_e32 v70, 2, v4
	v_xor_b32_e32 v4, 32, v2
	v_cmp_lt_i32_e32 vcc, v4, v3
	s_nop 1
	v_cndmask_b32_e32 v2, v2, v4, vcc
	v_lshlrev_b64 v[4:5], 2, v[24:25]
	v_lshlrev_b32_e32 v71, 2, v2
	v_lshl_add_u64 v[2:3], s[0:1], 0, v[4:5]
	v_lshl_add_u64 v[4:5], s[2:3], 0, v[4:5]
	s_mov_b64 s[0:1], 0x1000
	v_lshl_add_u64 v[6:7], v[2:3], 0, s[0:1]
	v_lshl_add_u64 v[8:9], v[4:5], 0, s[0:1]
	s_mov_b64 s[0:1], 0x1400
	s_lshl_b64 s[2:3], s[6:7], 2
	v_lshl_add_u64 v[10:11], v[2:3], 0, s[0:1]
	v_lshl_add_u64 v[12:13], v[4:5], 0, s[0:1]
	s_mov_b64 s[0:1], 0x1800
	s_add_u32 s18, s2, 0x518000
	v_lshl_add_u64 v[14:15], v[2:3], 0, s[0:1]
	v_lshl_add_u64 v[16:17], v[4:5], 0, s[0:1]
	s_mov_b64 s[0:1], 0x1c00
	s_addc_u32 s19, s3, 0
	s_ashr_i32 s9, s8, 31
	s_lshl_b64 s[2:3], s[6:7], 11
	v_lshl_add_u64 v[18:19], v[2:3], 0, s[0:1]
	v_lshl_add_u64 v[20:21], v[4:5], 0, s[0:1]
	v_cmp_eq_u32_e64 s[0:1], 0, v22
	s_lshl_b64 s[10:11], s[8:9], 2
	v_lshl_add_u64 v[22:23], s[12:13], 0, v[42:43]
	s_lshl_b64 s[12:13], s[8:9], 12
	v_lshl_add_u64 v[24:25], s[2:3], 0, v[24:25]
	s_lshl_b64 s[14:15], s[8:9], 11
	s_mov_b32 s7, 0xf800000
	s_mov_b32 s9, 0x42fe0000
	s_waitcnt vmcnt(0)
	s_branch .LBB0_638

.LBB0_1689:
	s_or_b64 exec, exec, s[4:5]
	v_cmp_gt_i32_e32 vcc, 16, v0
	v_lshl_add_u32 v81, v0, 2, 0
	s_and_saveexec_b64 s[4:5], vcc
	v_add_u32_e32 v2, 0x10000, v81
	v_mov_b32_e32 v3, 0
	ds_write_b32 v2, v3
	s_or_b64 exec, exec, s[4:5]
	s_abs_i32 s4, s87
	v_cvt_f32_u32_e32 v2, s4
	s_sub_i32 s7, 0, s4
	s_add_i32 s5, s87, 0x3fff
	s_xor_b32 s6, s5, s87
	v_rcp_iflag_f32_e32 v2, v2
	s_abs_i32 s5, s5
	s_ashr_i32 s6, s6, 31
	s_waitcnt lgkmcnt(0)
	v_mul_f32_e32 v2, 0x4f7ffffe, v2
	v_cvt_u32_f32_e32 v2, v2
	s_barrier
	v_readfirstlane_b32 s8, v2
	s_mul_i32 s7, s7, s8
	s_mul_hi_u32 s7, s8, s7
	s_add_i32 s8, s8, s7
	s_mul_hi_u32 s7, s5, s8
	s_mul_i32 s8, s7, s4
	s_sub_i32 s5, s5, s8
	s_add_i32 s9, s7, 1
	s_sub_i32 s8, s5, s4
	s_cmp_ge_u32 s5, s4
	s_cselect_b32 s7, s9, s7
	s_cselect_b32 s5, s8, s5
	s_add_i32 s8, s7, 1
	s_cmp_ge_u32 s5, s4
	s_cselect_b32 s4, s8, s7
	s_xor_b32 s4, s4, s6
	s_sub_i32 s4, s4, s6
	s_mul_i32 s33, s4, s90
	s_add_i32 s4, s33, s4
	s_min_i32 s34, s4, 0x4000
	s_add_i32 s18, s33, s89
	s_cmp_ge_i32 s18, s34
	s_cbranch_scc1 .LBB0_1698
	s_add_u32 s35, s66, 0x400000
	s_addc_u32 s36, s67, 0
	s_add_u32 s37, s66, 0x420000
	s_addc_u32 s38, s67, 0
	s_ashr_i32 s19, s18, 31
	s_lshl_b64 s[4:5], s[18:19], 12
	v_lshlrev_b32_e32 v24, 2, v80
	s_add_u32 s4, s64, s4
	v_ashrrev_i32_e32 v25, 31, v24
	s_addc_u32 s5, s65, s5
	v_lshlrev_b64 v[26:27], 1, v[24:25]
	v_lshl_add_u64 v[2:3], s[4:5], 0, v[26:27]
	global_load_dwordx2 v[36:37], v[2:3], off
	global_load_dwordx2 v[38:39], v[2:3], off offset:512
	global_load_dwordx2 v[40:41], v[2:3], off offset:1024
	global_load_dwordx2 v[28:29], v[2:3], off offset:1536
	global_load_dwordx2 v[34:35], v[2:3], off offset:2048
	global_load_dwordx2 v[42:43], v[2:3], off offset:2560
	global_load_dwordx2 v[32:33], v[2:3], off offset:3072
	global_load_dwordx2 v[30:31], v[2:3], off offset:3584
	v_mbcnt_lo_u32_b32 v4, -1, 0
	v_mbcnt_hi_u32_b32 v4, -1, v4
	v_and_b32_e32 v5, 64, v4
	v_add_u32_e32 v5, 64, v5
	v_xor_b32_e32 v6, 1, v4
	v_cmp_lt_i32_e32 vcc, v6, v5
	v_lshl_add_u64 v[2:3], s[64:65], 0, v[26:27]
	v_lshl_add_u32 v88, v80, 7, 0
	v_cndmask_b32_e32 v6, v4, v6, vcc
	v_lshlrev_b32_e32 v82, 2, v6
	v_xor_b32_e32 v6, 2, v4
	v_cmp_lt_i32_e32 vcc, v6, v5
	v_mov_b32_e32 v89, 0x3727c5ac
	s_mov_b32 s39, 0xf800000
	v_cndmask_b32_e32 v6, v4, v6, vcc
	v_lshlrev_b32_e32 v83, 2, v6
	v_xor_b32_e32 v6, 4, v4
	v_cmp_lt_i32_e32 vcc, v6, v5
	v_mov_b32_e32 v90, 0x260
	s_mov_b32 s40, 0x42fe0000
	v_cndmask_b32_e32 v6, v4, v6, vcc
	v_lshlrev_b32_e32 v84, 2, v6
	v_xor_b32_e32 v6, 8, v4
	v_cmp_lt_i32_e32 vcc, v6, v5
	s_mov_b32 s41, 0xc0c0400
	s_mov_b32 s42, 0x4000c0c
	v_cndmask_b32_e32 v6, v4, v6, vcc
	v_lshlrev_b32_e32 v85, 2, v6
	v_xor_b32_e32 v6, 16, v4
	v_cmp_lt_i32_e32 vcc, v6, v5
	v_mov_b32_e32 v91, 0
	s_mov_b32 s43, 0xff800000
	v_cndmask_b32_e32 v6, v4, v6, vcc
	v_lshlrev_b32_e32 v86, 2, v6
	v_xor_b32_e32 v6, 32, v4
	v_cmp_lt_i32_e32 vcc, v6, v5
	s_mov_b64 s[24:25], 0x4000
	s_mov_b64 s[26:27], 0x8000
	v_cndmask_b32_e32 v4, v4, v6, vcc
	v_lshlrev_b64 v[6:7], 2, v[24:25]
	v_lshl_add_u64 v[20:21], s[2:3], 0, v[6:7]
	s_mov_b64 s[2:3], 0x2000
	v_lshl_add_u64 v[22:23], s[0:1], 0, v[6:7]
	v_lshlrev_b32_e32 v87, 2, v4
	v_lshl_add_u64 v[4:5], v[20:21], 0, s[2:3]
	v_lshl_add_u64 v[6:7], v[22:23], 0, s[2:3]
	s_lshl_b32 s2, s89, 4
	s_add_i32 s2, s2, 0
	s_add_i32 s19, s2, 0x10040
	s_lshl_b32 s2, s33, 1
	s_lshl_b32 s3, s89, 1
	s_add_i32 s20, s2, s3
	s_ashr_i32 s3, s33, 31
	s_add_u32 s2, s89, s33
	s_addc_u32 s3, 0, s3
	s_lshl_b64 s[4:5], s[2:3], 2
	s_add_u32 s4, s66, s4
	s_addc_u32 s5, s67, s5
	s_add_u32 s22, s4, 0x518000
	s_addc_u32 s23, s5, 0
	s_lshl_b64 s[4:5], s[2:3], 11
	s_add_u32 s4, s66, s4
	s_mov_b64 s[0:1], 0x3000
	s_addc_u32 s5, s67, s5
	s_lshl_b64 s[2:3], s[2:3], 12
	v_lshl_add_u64 v[8:9], v[20:21], 0, s[0:1]
	v_lshl_add_u64 v[10:11], v[22:23], 0, s[0:1]
	s_mov_b64 s[0:1], 0x3400
	s_add_u32 s2, s66, s2
	v_lshl_add_u64 v[12:13], v[20:21], 0, s[0:1]
	v_lshl_add_u64 v[14:15], v[22:23], 0, s[0:1]
	s_mov_b64 s[0:1], 0x3800
	s_addc_u32 s3, s67, s3
	v_lshl_add_u64 v[16:17], v[20:21], 0, s[0:1]
	v_lshl_add_u64 v[18:19], v[22:23], 0, s[0:1]
	s_mov_b64 s[0:1], 0x3c00
	v_lshl_add_u64 v[24:25], s[4:5], 0, v[24:25]
	s_mov_b64 s[4:5], 0x38a00400
	v_lshl_add_u64 v[26:27], s[2:3], 0, v[26:27]
	s_mov_b64 s[2:3], 0x30a00800
	v_lshl_add_u64 v[20:21], v[20:21], 0, s[0:1]
	v_lshl_add_u64 v[22:23], v[22:23], 0, s[0:1]
	v_cmp_eq_u32_e64 s[0:1], 0, v80
	v_lshl_add_u64 v[24:25], v[24:25], 0, s[4:5]
	v_lshl_add_u64 v[26:27], v[26:27], 0, s[2:3]
	s_add_i32 s44, 0, 0x10000
	v_mov_b32_e32 v92, 0xff800000
	v_mov_b32_e32 v93, 1
	s_waitcnt vmcnt(0)
	s_branch .LBB0_1694

.LBB0_1694:
	s_waitcnt vmcnt(23)
	v_mov_b64_e32 v[52:53], v[36:37]
	s_waitcnt vmcnt(22)
	v_mov_b64_e32 v[62:63], v[38:39]
	s_waitcnt lgkmcnt(0)
	v_lshlrev_b32_e32 v59, 16, v52
	v_lshlrev_b32_e32 v58, 16, v62
	v_and_b32_e32 v61, 0xffff0000, v52
	v_and_b32_e32 v60, 0xffff0000, v62
	v_lshlrev_b32_e32 v55, 16, v53
	v_lshlrev_b32_e32 v54, 16, v63
	v_and_b32_e32 v57, 0xffff0000, v53
	v_and_b32_e32 v56, 0xffff0000, v63
	v_pk_add_f32 v[52:53], v[58:59], v[60:61]
	v_pk_add_f32 v[62:63], v[54:55], v[56:57]
	s_waitcnt vmcnt(21)
	v_mov_b64_e32 v[64:65], v[40:41]
	v_pk_add_f32 v[52:53], v[52:53], v[62:63]
	s_waitcnt vmcnt(20)
	v_lshlrev_b32_e32 v46, 16, v29
	v_and_b32_e32 v47, 0xffff0000, v29
	v_add_f32_e32 v29, 0, v53
	v_add_f32_e32 v49, v52, v29
	v_lshlrev_b32_e32 v53, 16, v65
	v_lshlrev_b32_e32 v52, 16, v64
	v_and_b32_e32 v65, 0xffff0000, v65
	v_and_b32_e32 v64, 0xffff0000, v64
	v_pk_add_f32 v[62:63], v[52:53], v[64:65]
	v_lshlrev_b32_e32 v44, 16, v28
	v_and_b32_e32 v45, 0xffff0000, v28
	v_pk_add_f32 v[62:63], v[62:63], v[62:63] op_sel_hi:[0,1]
	s_waitcnt vmcnt(18)
	v_mov_b64_e32 v[66:67], v[42:43]
	v_lshlrev_b32_e32 v42, 16, v34
	v_and_b32_e32 v50, 0xffff0000, v34
	v_lshlrev_b32_e32 v40, 16, v35
	v_and_b32_e32 v48, 0xffff0000, v35
	v_add_f32_e32 v43, v44, v45
	v_add_f32_e32 v51, v46, v47
	v_mov_b32_e32 v41, v63
	v_pk_add_f32 v[68:69], v[42:43], v[50:51]
	v_pk_add_f32 v[62:63], v[40:41], v[48:49]
	v_lshlrev_b32_e32 v73, 16, v67
	v_lshlrev_b32_e32 v72, 16, v66
	v_and_b32_e32 v67, 0xffff0000, v67
	v_and_b32_e32 v66, 0xffff0000, v66
	v_pk_add_f32 v[62:63], v[68:69], v[62:63]
	v_pk_add_f32 v[68:69], v[72:73], v[66:67]
	s_waitcnt vmcnt(17)
	v_lshlrev_b32_e32 v34, 16, v32
	v_and_b32_e32 v35, 0xffff0000, v32
	v_lshlrev_b32_e32 v38, 16, v33
	v_and_b32_e32 v39, 0xffff0000, v33
	v_pk_add_f32 v[62:63], v[62:63], v[62:63] op_sel_hi:[0,1]
	v_pk_add_f32 v[68:69], v[68:69], v[68:69] op_sel_hi:[0,1]
	s_waitcnt vmcnt(16)
	v_lshlrev_b32_e32 v32, 16, v30
	v_and_b32_e32 v36, 0xffff0000, v30
	v_lshlrev_b32_e32 v28, 16, v31
	v_and_b32_e32 v30, 0xffff0000, v31
	v_add_f32_e32 v33, v34, v35
	v_add_f32_e32 v37, v38, v39
	v_mov_b32_e32 v29, v69
	v_mov_b32_e32 v31, v63
	v_pk_add_f32 v[70:71], v[32:33], v[36:37]
	v_pk_add_f32 v[62:63], v[28:29], v[30:31]
	s_nop 0
	v_pk_add_f32 v[62:63], v[70:71], v[62:63]
	s_nop 0
	v_add_f32_e32 v29, v62, v63
	ds_bpermute_b32 v31, v82, v29
	s_waitcnt lgkmcnt(0)
	v_add_f32_e32 v29, v29, v31
	ds_bpermute_b32 v31, v83, v29
	s_waitcnt lgkmcnt(0)
	v_add_f32_e32 v29, v29, v31
	ds_bpermute_b32 v31, v84, v29
	s_waitcnt lgkmcnt(0)
	v_add_f32_e32 v29, v29, v31
	ds_bpermute_b32 v31, v85, v29
	s_waitcnt lgkmcnt(0)
	v_add_f32_e32 v29, v29, v31
	ds_bpermute_b32 v31, v86, v29
	s_waitcnt lgkmcnt(0)
	v_add_f32_e32 v29, v29, v31
	ds_bpermute_b32 v31, v87, v29
	s_waitcnt lgkmcnt(0)
	v_add_f32_e32 v29, v29, v31
	v_fmac_f32_e32 v61, 0xba000000, v29
	v_fmac_f32_e32 v60, 0xba000000, v29
	v_fmac_f32_e32 v57, 0xba000000, v29
	v_fmac_f32_e32 v59, 0xba000000, v29
	v_fmac_f32_e32 v56, 0xba000000, v29
	v_fmac_f32_e32 v58, 0xba000000, v29
	v_mov_b32_e32 v68, v61
	v_mov_b32_e32 v69, v60
	v_fmac_f32_e32 v55, 0xba000000, v29
	v_fmac_f32_e32 v54, 0xba000000, v29
	v_mov_b32_e32 v62, v59
	v_mov_b32_e32 v63, v58
	v_pk_mul_f32 v[68:69], v[68:69], v[68:69]
	v_mov_b32_e32 v70, v57
	v_mov_b32_e32 v71, v56
	v_pk_fma_f32 v[62:63], v[62:63], v[62:63], v[68:69]
	v_mov_b32_e32 v68, v55
	v_mov_b32_e32 v69, v54
	v_pk_mul_f32 v[70:71], v[70:71], v[70:71]
	v_fmac_f32_e32 v64, 0xba000000, v29
	v_pk_fma_f32 v[68:69], v[68:69], v[68:69], v[70:71]
	v_fmac_f32_e32 v65, 0xba000000, v29
	v_pk_add_f32 v[62:63], v[62:63], v[68:69]
	v_fmac_f32_e32 v53, 0xba000000, v29
	v_pk_add_f32 v[68:69], v[62:63], v[62:63] op_sel_hi:[0,1]
	v_fmac_f32_e32 v52, 0xba000000, v29
	v_mov_b32_e32 v62, v53
	v_mov_b32_e32 v63, v65
	v_mov_b32_e32 v53, v64
	v_pk_mul_f32 v[70:71], v[62:63], v[62:63]
	v_pk_mul_f32 v[64:65], v[52:53], v[52:53]
	v_fmac_f32_e32 v44, 0xba000000, v29
	v_pk_mov_b32 v[74:75], v[64:65], v[70:71] op_sel:[1,0]
	v_mov_b32_e32 v65, v71
	v_pk_add_f32 v[64:65], v[74:75], v[64:65]
	v_fmac_f32_e32 v45, 0xba000000, v29
	v_pk_add_f32 v[64:65], v[64:65], v[64:65] op_sel_hi:[0,1]
	v_fmac_f32_e32 v46, 0xba000000, v29
	v_mul_f32_e32 v64, v44, v44
	v_fmac_f32_e32 v47, 0xba000000, v29
	v_pk_fma_f32 v[70:71], v[44:45], v[44:45], v[64:65] op_sel_hi:[1,1,0]
	v_mul_f32_e32 v64, v46, v46
	v_pk_fma_f32 v[74:75], v[46:47], v[46:47], v[64:65] op_sel_hi:[1,1,0]
	v_fmac_f32_e32 v48, 0xba000000, v29
	v_fmac_f32_e32 v40, 0xba000000, v29
	v_fmac_f32_e32 v50, 0xba000000, v29
	v_fmac_f32_e32 v42, 0xba000000, v29
	v_mul_f32_e32 v70, v42, v42
	v_mul_f32_e32 v74, v50, v50
	v_mul_f32_e32 v64, v40, v40
	v_mul_f32_e32 v68, v48, v48
	v_pk_add_f32 v[70:71], v[70:71], v[74:75]
	v_pk_add_f32 v[64:65], v[64:65], v[68:69]
	v_fmac_f32_e32 v66, 0xba000000, v29
	v_fmac_f32_e32 v67, 0xba000000, v29
	v_fmac_f32_e32 v73, 0xba000000, v29
	v_pk_add_f32 v[64:65], v[70:71], v[64:65]
	v_fmac_f32_e32 v72, 0xba000000, v29
	v_mov_b32_e32 v78, v73
	v_mov_b32_e32 v79, v67
	v_mov_b32_e32 v73, v66
	v_pk_add_f32 v[64:65], v[64:65], v[64:65] op_sel_hi:[0,1]
	v_pk_mul_f32 v[68:69], v[78:79], v[78:79]
	v_pk_mul_f32 v[66:67], v[72:73], v[72:73]
	v_fmac_f32_e32 v34, 0xba000000, v29
	v_pk_mov_b32 v[70:71], v[66:67], v[68:69] op_sel:[1,0]
	v_mov_b32_e32 v67, v69
	v_fmac_f32_e32 v35, 0xba000000, v29
	v_fmac_f32_e32 v38, 0xba000000, v29
	v_mul_f32_e32 v64, v34, v34
	v_pk_add_f32 v[66:67], v[70:71], v[66:67]
	v_fmac_f32_e32 v39, 0xba000000, v29
	v_pk_fma_f32 v[68:69], v[34:35], v[34:35], v[64:65] op_sel_hi:[1,1,0]
	v_mul_f32_e32 v64, v38, v38
	v_pk_add_f32 v[66:67], v[66:67], v[66:67] op_sel_hi:[0,1]
	v_pk_fma_f32 v[70:71], v[38:39], v[38:39], v[64:65] op_sel_hi:[1,1,0]
	v_fmac_f32_e32 v30, 0xba000000, v29
	v_fmac_f32_e32 v28, 0xba000000, v29
	v_fmac_f32_e32 v36, 0xba000000, v29
	v_fmac_f32_e32 v32, 0xba000000, v29
	v_mul_f32_e32 v68, v32, v32
	v_mul_f32_e32 v70, v36, v36
	v_mul_f32_e32 v66, v28, v28
	v_mul_f32_e32 v64, v30, v30
	v_pk_add_f32 v[68:69], v[68:69], v[70:71]
	v_pk_add_f32 v[64:65], v[66:67], v[64:65]
	v_mov_b32_e32 v151, v60
	v_pk_add_f32 v[64:65], v[68:69], v[64:65]
	v_mov_b32_e32 v60, v59
	v_add_f32_e32 v29, v64, v65
	global_load_dwordx4 v[64:67], v[4:5], off
	global_load_dwordx4 v[68:71], v[6:7], off
	global_load_dwordx4 v[94:97], v[4:5], off offset:1024
	global_load_dwordx4 v[98:101], v[6:7], off offset:1024
	global_load_dwordx4 v[102:105], v[4:5], off offset:2048
	global_load_dwordx4 v[106:109], v[6:7], off offset:2048
	global_load_dwordx4 v[110:113], v[4:5], off offset:3072
	global_load_dwordx4 v[114:117], v[6:7], off offset:3072
	global_load_dwordx4 v[118:121], v[8:9], off
	global_load_dwordx4 v[122:125], v[10:11], off
	global_load_dwordx4 v[126:129], v[12:13], off
	global_load_dwordx4 v[130:133], v[14:15], off
	global_load_dwordx4 v[134:137], v[16:17], off
	global_load_dwordx4 v[138:141], v[18:19], off
	global_load_dwordx4 v[142:145], v[20:21], off
	global_load_dwordx4 v[146:149], v[22:23], off
	ds_bpermute_b32 v31, v82, v29
	v_mov_b32_e32 v59, v56
	v_mov_b32_e32 v56, v55
	v_mov_b32_e32 v150, v58
	v_mov_b32_e32 v58, v54
	s_waitcnt lgkmcnt(0)
	v_add_f32_e32 v29, v29, v31
	ds_bpermute_b32 v31, v83, v29
	s_waitcnt lgkmcnt(0)
	v_add_f32_e32 v29, v29, v31
	ds_bpermute_b32 v31, v84, v29
	s_waitcnt lgkmcnt(0)
	v_add_f32_e32 v29, v29, v31
	ds_bpermute_b32 v31, v85, v29
	s_waitcnt lgkmcnt(0)
	v_add_f32_e32 v29, v29, v31
	ds_bpermute_b32 v31, v86, v29
	s_waitcnt lgkmcnt(0)
	v_add_f32_e32 v29, v29, v31
	ds_bpermute_b32 v31, v87, v29
	s_waitcnt lgkmcnt(0)
	v_add_f32_e32 v29, v29, v31
	v_fmamk_f32 v29, v29, 0x3a000000, v89
	v_mul_f32_e32 v31, 0x4f800000, v29
	v_cmp_gt_f32_e32 vcc, s39, v29
	s_nop 1
	v_cndmask_b32_e32 v29, v29, v31, vcc
	v_sqrt_f32_e32 v31, v29
	s_nop 0
	v_add_u32_e32 v33, -1, v31
	v_fma_f32 v37, -v33, v31, v29
	v_cmp_ge_f32_e64 s[2:3], 0, v37
	v_add_u32_e32 v37, 1, v31
	s_nop 0
	v_cndmask_b32_e64 v33, v31, v33, s[2:3]
	v_fma_f32 v31, -v37, v31, v29
	v_cmp_lt_f32_e64 s[2:3], 0, v31
	s_nop 1
	v_cndmask_b32_e64 v31, v33, v37, s[2:3]
	v_mul_f32_e32 v33, 0x37800000, v31
	v_cndmask_b32_e32 v31, v31, v33, vcc
	v_cmp_class_f32_e32 vcc, v29, v90
	s_nop 1
	v_cndmask_b32_e32 v29, v31, v29, vcc
	v_div_scale_f32 v31, s[2:3], v29, v29, 1.0
	v_rcp_f32_e32 v33, v31
	s_mov_b32 s2, s18
	s_add_i32 s18, s18, 8
	s_cmp_ge_i32 s18, s34
	v_fma_f32 v37, -v31, v33, 1.0
	v_fmac_f32_e32 v33, v37, v33
	v_div_scale_f32 v37, vcc, 1.0, v29, 1.0
	v_mul_f32_e32 v41, v37, v33
	v_fma_f32 v43, -v31, v41, v37
	v_fmac_f32_e32 v41, v43, v33
	v_fma_f32 v31, -v31, v41, v37
	v_div_fmas_f32 v31, v31, v33, v41
	v_div_fixup_f32 v152, v31, v29, 1.0
	v_pk_mul_f32 v[54:55], v[60:61], v[152:153] op_sel_hi:[1,0]
	v_pk_mul_f32 v[56:57], v[56:57], v[152:153] op_sel_hi:[1,0]
	v_mov_b32_e32 v29, v30
	s_waitcnt vmcnt(14)
	v_pk_fma_f32 v[74:75], v[66:67], v[56:57], v[70:71]
	v_pk_fma_f32 v[76:77], v[64:65], v[54:55], v[68:69]
	v_pk_mul_f32 v[54:55], v[150:151], v[152:153] op_sel_hi:[1,0]
	v_pk_mul_f32 v[56:57], v[58:59], v[152:153] op_sel_hi:[1,0]
	v_pk_mul_f32 v[44:45], v[44:45], v[152:153] op_sel_hi:[1,0]
	v_pk_mul_f32 v[28:29], v[28:29], v[152:153] op_sel_hi:[1,0]
	s_waitcnt vmcnt(12)
	v_pk_fma_f32 v[66:67], v[96:97], v[56:57], v[100:101]
	v_pk_fma_f32 v[70:71], v[94:95], v[54:55], v[98:99]
	v_pk_mul_f32 v[52:53], v[52:53], v[152:153] op_sel_hi:[1,0]
	v_pk_mul_f32 v[54:55], v[62:63], v[152:153] op_sel_hi:[1,0]
	s_waitcnt vmcnt(8)
	v_pk_fma_f32 v[64:65], v[110:111], v[44:45], v[114:115]
	s_waitcnt vmcnt(0)
	v_pk_fma_f32 v[44:45], v[144:145], v[28:29], v[148:149]
	v_max_f32_e64 v28, |v76|, |v77|
	v_max_f32_e64 v29, |v74|, |v75|
	v_pk_fma_f32 v[62:63], v[104:105], v[54:55], v[108:109]
	v_pk_fma_f32 v[68:69], v[102:103], v[52:53], v[106:107]
	v_pk_mul_f32 v[46:47], v[46:47], v[152:153] op_sel_hi:[1,0]
	v_mov_b32_e32 v43, v50
	v_mov_b32_e32 v41, v48
	v_max3_f32 v28, v28, 0, v29
	v_max_f32_e64 v29, |v70|, |v71|
	v_max_f32_e64 v30, |v66|, |v67|
	v_pk_fma_f32 v[60:61], v[112:113], v[46:47], v[116:117]
	v_pk_mul_f32 v[42:43], v[42:43], v[152:153] op_sel_hi:[1,0]
	v_pk_mul_f32 v[40:41], v[40:41], v[152:153] op_sel_hi:[1,0]
	v_max3_f32 v28, v28, v29, v30
	v_max_f32_e64 v29, |v68|, |v69|
	v_max_f32_e64 v30, |v62|, |v63|
	v_pk_fma_f32 v[54:55], v[120:121], v[40:41], v[124:125]
	v_pk_fma_f32 v[58:59], v[118:119], v[42:43], v[122:123]
	v_pk_mul_f32 v[40:41], v[72:73], v[152:153] op_sel_hi:[1,0]
	v_pk_mul_f32 v[42:43], v[78:79], v[152:153] op_sel_hi:[1,0]
	v_max3_f32 v28, v28, v29, v30
	v_max_f32_e64 v29, |v64|, |v65|
	v_max_f32_e64 v30, |v60|, |v61|
	v_pk_fma_f32 v[52:53], v[128:129], v[42:43], v[132:133]
	v_pk_fma_f32 v[56:57], v[126:127], v[40:41], v[130:131]
	v_pk_mul_f32 v[34:35], v[34:35], v[152:153] op_sel_hi:[1,0]
	v_pk_mul_f32 v[38:39], v[38:39], v[152:153] op_sel_hi:[1,0]
	v_mov_b32_e32 v33, v36
	v_max3_f32 v28, v28, v29, v30
	v_max_f32_e64 v29, |v58|, |v59|
	v_max_f32_e64 v30, |v54|, |v55|
	v_pk_fma_f32 v[46:47], v[136:137], v[38:39], v[140:141]
	v_pk_fma_f32 v[50:51], v[134:135], v[34:35], v[138:139]
	v_pk_mul_f32 v[32:33], v[32:33], v[152:153] op_sel_hi:[1,0]
	v_max3_f32 v28, v28, v29, v30
	v_max_f32_e64 v29, |v56|, |v57|
	v_max_f32_e64 v30, |v52|, |v53|
	v_pk_fma_f32 v[48:49], v[142:143], v[32:33], v[146:147]
	v_max3_f32 v28, v28, v29, v30
	v_max_f32_e64 v29, |v50|, |v51|
	v_max_f32_e64 v30, |v46|, |v47|
	v_max3_f32 v28, v28, v29, v30
	v_max_f32_e64 v29, |v48|, |v49|
	v_max_f32_e64 v30, |v44|, |v45|
	v_max3_f32 v28, v28, v29, v30
	ds_bpermute_b32 v29, v82, v28
	s_cselect_b64 s[28:29], -1, 0
	s_cmp_lt_i32 s18, s34
	s_cselect_b32 s2, s18, s2
	s_ashr_i32 s3, s2, 31
	s_waitcnt lgkmcnt(0)
	v_max_f32_e32 v29, v29, v29
	v_max_f32_e32 v28, v28, v29
	ds_bpermute_b32 v29, v83, v28
	s_lshl_b64 s[2:3], s[2:3], 12
	v_lshl_add_u64 v[30:31], v[2:3], 0, s[2:3]
	s_waitcnt lgkmcnt(0)
	v_max_f32_e32 v29, v29, v29
	v_max_f32_e32 v28, v28, v29
	ds_bpermute_b32 v29, v84, v28
	s_waitcnt lgkmcnt(0)
	v_max_f32_e32 v29, v29, v29
	v_max_f32_e32 v28, v28, v29
	ds_bpermute_b32 v29, v85, v28
	s_waitcnt lgkmcnt(0)
	v_max_f32_e32 v29, v29, v29
	v_max_f32_e32 v28, v28, v29
	ds_bpermute_b32 v29, v86, v28
	s_waitcnt lgkmcnt(0)
	v_max_f32_e32 v29, v29, v29
	v_max_f32_e32 v32, v28, v29
	ds_bpermute_b32 v33, v87, v32
	global_load_dwordx2 v[36:37], v[30:31], off
	global_load_dwordx2 v[38:39], v[30:31], off offset:512
	global_load_dwordx2 v[40:41], v[30:31], off offset:1024
	global_load_dwordx2 v[28:29], v[30:31], off offset:1536
	s_waitcnt lgkmcnt(0)
	v_max_f32_e32 v33, v33, v33
	v_max_f32_e32 v72, v32, v33
	global_load_dwordx2 v[34:35], v[30:31], off offset:2048
	global_load_dwordx2 v[42:43], v[30:31], off offset:2560
	global_load_dwordx2 v[32:33], v[30:31], off offset:3072
	s_nop 0
	global_load_dwordx2 v[30:31], v[30:31], off offset:3584
	v_div_scale_f32 v73, s[2:3], v72, v72, s40
	v_rcp_f32_e32 v78, v73
	s_nop 0
	v_fma_f32 v79, -v73, v78, 1.0
	v_fmac_f32_e32 v78, v79, v78
	v_div_scale_f32 v79, vcc, s40, v72, s40
	v_mul_f32_e32 v94, v79, v78
	v_fma_f32 v95, -v73, v94, v79
	v_fmac_f32_e32 v94, v95, v78
	v_fma_f32 v73, -v73, v94, v79
	v_div_fmas_f32 v73, v73, v78, v94
	v_div_fixup_f32 v73, v73, v72, s40
	v_cmp_lt_f32_e32 vcc, 0, v72
	v_cvt_pk_bf16_f32 v78, v76, v77
	v_cvt_pk_bf16_f32 v79, v74, v75
	global_store_dwordx2 v[26:27], v[78:79], off offset:-2048
	s_nop 0
	v_cndmask_b32_e32 v73, 0, v73, vcc
	v_fmaak_f32 v78, v76, v73, 0x4b400000
	v_fmaak_f32 v79, v77, v73, 0x4b400000
	v_fmaak_f32 v94, v74, v73, 0x4b400000
	v_fmaak_f32 v95, v75, v73, 0x4b400000
	v_perm_b32 v78, v79, v78, s41
	v_perm_b32 v79, v95, v94, s42
	v_or_b32_e32 v78, v79, v78
	global_store_dword v[24:25], v78, off offset:-1024
	v_cvt_pk_bf16_f32 v78, v70, v71
	v_cvt_pk_bf16_f32 v79, v66, v67
	global_store_dwordx2 v[26:27], v[78:79], off offset:-1536
	v_fmaak_f32 v78, v70, v73, 0x4b400000
	v_fmaak_f32 v79, v71, v73, 0x4b400000
	v_fmaak_f32 v94, v66, v73, 0x4b400000
	v_fmaak_f32 v95, v67, v73, 0x4b400000
	v_perm_b32 v78, v79, v78, s41
	v_perm_b32 v79, v95, v94, s42
	v_or_b32_e32 v78, v79, v78
	global_store_dword v[24:25], v78, off offset:-768
	v_cvt_pk_bf16_f32 v78, v68, v69
	v_cvt_pk_bf16_f32 v79, v62, v63
	global_store_dwordx2 v[26:27], v[78:79], off offset:-1024
	v_fmaak_f32 v78, v68, v73, 0x4b400000
	v_fmaak_f32 v79, v69, v73, 0x4b400000
	v_fmaak_f32 v94, v62, v73, 0x4b400000
	v_fmaak_f32 v95, v63, v73, 0x4b400000
	v_perm_b32 v78, v79, v78, s41
	v_perm_b32 v79, v95, v94, s42
	v_or_b32_e32 v78, v79, v78
	global_store_dword v[24:25], v78, off offset:-512
	v_cvt_pk_bf16_f32 v78, v64, v65
	v_cvt_pk_bf16_f32 v79, v60, v61
	global_store_dwordx2 v[26:27], v[78:79], off offset:-512
	v_fmaak_f32 v78, v64, v73, 0x4b400000
	v_fmaak_f32 v79, v65, v73, 0x4b400000
	v_fmaak_f32 v94, v60, v73, 0x4b400000
	v_fmaak_f32 v95, v61, v73, 0x4b400000
	v_perm_b32 v78, v79, v78, s41
	v_perm_b32 v79, v95, v94, s42
	v_or_b32_e32 v78, v79, v78
	global_store_dword v[24:25], v78, off offset:-256
	v_cvt_pk_bf16_f32 v78, v58, v59
	v_cvt_pk_bf16_f32 v79, v54, v55
	global_store_dwordx2 v[26:27], v[78:79], off
	v_fmaak_f32 v78, v58, v73, 0x4b400000
	v_fmaak_f32 v79, v59, v73, 0x4b400000
	v_fmaak_f32 v94, v54, v73, 0x4b400000
	v_fmaak_f32 v95, v55, v73, 0x4b400000
	v_perm_b32 v78, v79, v78, s41
	v_perm_b32 v79, v95, v94, s42
	v_or_b32_e32 v78, v79, v78
	global_store_dword v[24:25], v78, off
	v_cvt_pk_bf16_f32 v78, v56, v57
	v_cvt_pk_bf16_f32 v79, v52, v53
	global_store_dwordx2 v[26:27], v[78:79], off offset:512
	v_fmaak_f32 v78, v56, v73, 0x4b400000
	v_fmaak_f32 v79, v57, v73, 0x4b400000
	v_fmaak_f32 v94, v52, v73, 0x4b400000
	v_fmaak_f32 v95, v53, v73, 0x4b400000
	v_perm_b32 v78, v79, v78, s41
	v_perm_b32 v79, v95, v94, s42
	v_or_b32_e32 v78, v79, v78
	global_store_dword v[24:25], v78, off offset:256
	v_cvt_pk_bf16_f32 v78, v50, v51
	v_cvt_pk_bf16_f32 v79, v46, v47
	global_store_dwordx2 v[26:27], v[78:79], off offset:1024
	v_fmaak_f32 v78, v50, v73, 0x4b400000
	v_fmaak_f32 v79, v51, v73, 0x4b400000
	v_fmaak_f32 v94, v46, v73, 0x4b400000
	v_fmaak_f32 v95, v47, v73, 0x4b400000
	v_perm_b32 v78, v79, v78, s41
	v_perm_b32 v79, v95, v94, s42
	v_or_b32_e32 v78, v79, v78
	global_store_dword v[24:25], v78, off offset:512
	v_cvt_pk_bf16_f32 v78, v48, v49
	v_cvt_pk_bf16_f32 v79, v44, v45
	global_store_dwordx2 v[26:27], v[78:79], off offset:1536
	v_fmaak_f32 v78, v48, v73, 0x4b400000
	v_fmaak_f32 v79, v49, v73, 0x4b400000
	v_fmaak_f32 v94, v44, v73, 0x4b400000
	v_fmaak_f32 v73, v45, v73, 0x4b400000
	v_perm_b32 v78, v79, v78, s41
	v_perm_b32 v73, v73, v94, s42
	v_or_b32_e32 v73, v73, v78
	global_store_dword v[24:25], v73, off offset:768
	s_and_saveexec_b64 s[2:3], s[0:1]
	s_cbranch_execz .LBB0_1696
	v_mul_f32_e32 v72, 0x3c010204, v72
	v_cndmask_b32_e32 v72, 1.0, v72, vcc
	global_store_dword v91, v72, s[22:23]
